# conversion order: each of the 96 converting workgroups takes two adjacent tile pairs in a row (same source rows) before striding
# speedup vs baseline: 1.0350x; 1.0018x over previous
; #define PW_SYNC do { asm volatile("s_waitcnt lgkmcnt(0)" ::: "memory"); __builtin_amdgcn_s_barrier(); asm volatile("" ::: "memory"); } while (0)
; __device__ __forceinline__ void ph_weights(const Params& p, LAS unsigned char* lds, const int p0, const int p1, const int wi, const int wn) {
;     ...
;     int pi = p0 + wi; bool hA, hB;
;     PW_LOAD(pi, dA0, dA1, a0, a1, hA);
;     PW_LOAD(pi + wn, dB0, dB1, b0, b1, hB);
;     while (hA) {
;         { PW_TOLDS(dA0, a0, a1); PW_SYNC; const TDesc s0 = dA0, s1 = dA1; PW_LOAD(pi + 2 * wn, dA0, dA1, a0, a1, hA); PW_STORE(s0, s1); PW_SYNC; }
;         if (!hB) break;
;         { PW_TOLDS(dB0, b0, b1); PW_SYNC; const TDesc s0 = dB0, s1 = dB1; PW_LOAD(pi + 3 * wn, dB0, dB1, b0, b1, hB); PW_STORE(s0, s1); PW_SYNC; }
;         pi += 2 * wn;
.LBB0_779:
	v_readlane_b32 s0, v249, 28
	s_nop 3
	s_mul_i32 s0, s0, 2
	s_add_u32 s0, s0, 4294967216
	s_movk_i32 s70, 190
	s_movk_i32 s73, 2
	s_movk_i32 s71, 0x16b0
	s_mov_b32 s74, 0
	v_writelane_b32 v255, s29, 61
	s_branch .Lcv_common
.Lcv_late:
	v_readlane_b32 s0, v249, 28
	s_nop 3
	s_mul_i32 s0, s0, 1
	s_add_u32 s0, s0, 5680
	s_movk_i32 s70, 31
	s_movk_i32 s73, 1
	s_movk_i32 s71, 0x1920
	s_mov_b32 s74, 0
	v_writelane_b32 v255, s29, 61
	s_branch .Lcv_common
.Lcv_idle:
	v_writelane_b32 v246, s14, 0
	v_writelane_b32 v246, s15, 1
	v_writelane_b32 v246, s20, 2
	v_writelane_b32 v246, s21, 3
	v_writelane_b32 v246, s29, 4
	v_writelane_b32 v246, s30, 5
	v_writelane_b32 v246, s31, 6
	v_writelane_b32 v246, s36, 7
	v_writelane_b32 v246, s37, 8
	v_writelane_b32 v246, s56, 9
	v_writelane_b32 v246, s57, 10
	v_writelane_b32 v246, s69, 11
	s_mov_b32 s74, 1
	s_waitcnt vmcnt(0) lgkmcnt(0)
	s_barrier
	v_readlane_b32 s0, v249, 28
	s_nop 3
	s_mul_i32 s0, s0, 1
	s_add_u32 s0, s0, 6464
	s_movk_i32 s70, 31
	s_movk_i32 s73, 1
	s_movk_i32 s71, 0x1ae0
	s_branch .Lcv_common
.Lcv_tail:
	v_writelane_b32 v246, s14, 0
	v_writelane_b32 v246, s15, 1
	v_writelane_b32 v246, s20, 2
	v_writelane_b32 v246, s21, 3
	v_writelane_b32 v246, s29, 4
	v_writelane_b32 v246, s30, 5
	v_writelane_b32 v246, s31, 6
	v_writelane_b32 v246, s36, 7
	v_writelane_b32 v246, s37, 8
	v_writelane_b32 v246, s56, 9
	v_writelane_b32 v246, s57, 10
	v_writelane_b32 v246, s69, 11
	s_mov_b32 s74, 2
	s_waitcnt vmcnt(0) lgkmcnt(0)
	s_barrier
	v_readlane_b32 s0, v249, 28
	s_nop 3
	s_mul_i32 s0, s0, 1
	s_add_u32 s0, s0, 6432
	s_movk_i32 s70, 127
	s_movk_i32 s73, 1
	s_movk_i32 s71, 0x1a20
.Lcv_common:
	s_mov_b32 s72, 0
	s_waitcnt lgkmcnt(0)
	v_and_b32_e32 v166, 31, v0
	v_lshrrev_b32_e32 v167, 5, v0
	v_lshlrev_b32_e32 v168, 1, v167
	v_lshlrev_b32_e32 v169, 4, v166
	v_lshlrev_b32_e32 v170, 3, v167
	v_lshrrev_b32_e32 v1, 2, v167
	v_lshlrev_b32_e32 v1, 4, v1
	v_xor_b32_e32 v1, v169, v1
	v_lshl_add_u32 v154, v167, 9, v1
	v_xor_b32_e32 v155, 64, v154
	v_xor_b32_e32 v156, 0x80, v154
	v_xor_b32_e32 v157, 0xc0, v154
	v_and_b32_e32 v171, 15, v0
	v_lshrrev_b32_e32 v175, 4, v0
	v_lshlrev_b32_e32 v1, 2, v171
	v_xor_b32_e32 v1, v175, v1
	v_lshlrev_b32_e32 v174, 11, v171
	v_lshl_add_u32 v162, v1, 2, v174
	v_xor_b32_e32 v163, 0x80, v162
	v_xor_b32_e32 v164, 0x100, v162
	v_xor_b32_e32 v165, 0x180, v162
	v_lshlrev_b32_e32 v176, 4, v171
	v_add_u32_e32 v158, 0x10000, v154
	v_add_u32_e32 v159, 0x10000, v155
	v_add_u32_e32 v160, 0x10000, v156
	v_add_u32_e32 v161, 0x10000, v157
	v_add_u32_e32 v130, 0x10000, v162
	v_add_u32_e32 v131, 0x10000, v163
	v_add_u32_e32 v132, 0x10000, v164
	v_add_u32_e32 v133, 0x10000, v165
	s_mov_b32 s9, 3
	s_mov_b32 s86, s0
	s_add_u32 s0, s0, 1
	s_add_u32 s72, s72, 1
	s_cmp_eq_u32 s72, s73
	s_cselect_b32 s8, s70, 0
	s_cselect_b32 s72, 0, s72
	s_add_u32 s0, s0, s8
	s_cmp_ge_u32 s86, 0xd70
	s_cselect_b32 s77, 1, 0
	s_mul_i32 s83, s77, 0xd70
	s_sub_u32 s78, s86, s83
	v_readlane_b32 s20, v249, 37
	v_readlane_b32 s21, v249, 38
	s_mov_b32 s29, 0
	s_cmpk_lt_u32 s78, 0xf0
	s_cbranch_scc1 .Lcv_win_A1
	s_cmpk_lt_u32 s78, 0x170
	s_cbranch_scc1 .Lcv_wout_A1
	s_cmpk_lt_u32 s78, 0x970
	s_cbranch_scc1 .Lcv_gu_A1
	s_sub_u32 s78, s78, 0x970
	s_lshr_b32 s83, s78, 6
	s_bfe_u32 s93, s78, 0x30003
	s_and_b32 s94, s78, 7
	s_mul_i32 s98, s77, 0x8000000
	s_lshl_b32 s95, s83, 23
	s_add_u32 s98, s98, s95
	s_lshl_b32 s95, s93, 20
	s_add_u32 s98, s98, s95
	s_lshl_b32 s95, s94, 10
	s_add_u32 s98, s98, s95
	s_mul_i32 s99, s77, 0x4000000
	s_add_u32 s99, s99, 0x14400000
	s_lshl_b32 s95, s83, 22
	s_add_u32 s99, s99, s95
	s_lshl_b32 s95, s94, 19
	s_add_u32 s99, s99, s95
	s_lshl_b32 s95, s93, 8
	s_add_u32 s99, s99, s95
	v_readlane_b32 s12, v249, 4
	v_readlane_b32 s13, v249, 5
	s_movk_i32 s22, 0x2000
	s_movk_i32 s23, 0x800
	s_mov_b32 s28, 0x40000
	s_branch .Lcv_fin_A1

; __device__ __forceinline__ void ph_weights(const Params& p, LAS unsigned char* lds, const int p0, const int p1, const int wi, const int wn) {
;     ...
;     int pi = p0 + wi; bool hA, hB;
;     PW_LOAD(pi, dA0, dA1, a0, a1, hA);
;     PW_LOAD(pi + wn, dB0, dB1, b0, b1, hB);
.Lcv_fin_A1:
	s_nop 3
	s_add_u32 s12, s12, s98
	s_addc_u32 s13, s13, 0
	s_add_u32 s14, s26, s99
	s_addc_u32 s15, s27, 0
	v_mad_u32_u24 v177, v168, s22, v169
	s_mov_b64 s[88:89], s[12:13]
	s_add_u32 s90, s12, s22
	s_addc_u32 s91, s13, 0
	s_lshl_b32 s92, s22, 5
	global_load_dwordx2 v[138:139], v170, s[20:21]
	global_load_dwordx2 v[140:141], v170, s[20:21] offset:128
	global_load_dwordx2 v[142:143], v170, s[20:21] offset:256
	global_load_dwordx2 v[144:145], v170, s[20:21] offset:384
	global_load_dwordx4 v[2:5], v177, s[88:89] nt
	global_load_dwordx4 v[34:37], v177, s[88:89] offset:512 nt
	global_load_dwordx4 v[6:9], v177, s[90:91] nt
	global_load_dwordx4 v[38:41], v177, s[90:91] offset:512 nt
	s_add_u32 s88, s88, s92
	s_addc_u32 s89, s89, 0
	s_add_u32 s90, s90, s92
	s_addc_u32 s91, s91, 0
	global_load_dwordx4 v[10:13], v177, s[88:89] nt
	global_load_dwordx4 v[42:45], v177, s[88:89] offset:512 nt
	global_load_dwordx4 v[14:17], v177, s[90:91] nt
	global_load_dwordx4 v[46:49], v177, s[90:91] offset:512 nt
	s_add_u32 s88, s88, s92
	s_addc_u32 s89, s89, 0
	s_add_u32 s90, s90, s92
	s_addc_u32 s91, s91, 0
	global_load_dwordx4 v[18:21], v177, s[88:89] nt
	global_load_dwordx4 v[50:53], v177, s[88:89] offset:512 nt
	global_load_dwordx4 v[22:25], v177, s[90:91] nt
	global_load_dwordx4 v[54:57], v177, s[90:91] offset:512 nt
	s_add_u32 s88, s88, s92
	s_addc_u32 s89, s89, 0
	s_add_u32 s90, s90, s92
	s_addc_u32 s91, s91, 0
	global_load_dwordx4 v[26:29], v177, s[88:89] nt
	global_load_dwordx4 v[58:61], v177, s[88:89] offset:512 nt
	global_load_dwordx4 v[30:33], v177, s[90:91] nt
	global_load_dwordx4 v[62:65], v177, s[90:91] offset:512 nt
	global_load_dword v1, v170, s[20:21]
	global_load_dword v1, v170, s[20:21]
	global_load_dword v1, v170, s[20:21]
	global_load_dword v1, v170, s[20:21]
	global_load_dword v1, v170, s[20:21]
	global_load_dword v1, v170, s[20:21]
	global_load_dword v1, v170, s[20:21]
	global_load_dword v1, v170, s[20:21]
	s_mov_b32 s86, s0
	s_add_u32 s0, s0, 1
	s_add_u32 s72, s72, 1
	s_cmp_eq_u32 s72, s73
	s_cselect_b32 s8, s70, 0
	s_cselect_b32 s72, 0, s72
	s_add_u32 s0, s0, s8
	s_cmp_ge_u32 s86, 0xd70
	s_cselect_b32 s77, 1, 0
	s_mul_i32 s83, s77, 0xd70
	s_sub_u32 s78, s86, s83
	v_readlane_b32 s36, v249, 37
	v_readlane_b32 s37, v249, 38
	s_mov_b32 s60, 0
	s_cmpk_lt_u32 s78, 0xf0
	s_cbranch_scc1 .Lcv_win_B2
	s_cmpk_lt_u32 s78, 0x170
	s_cbranch_scc1 .Lcv_wout_B2
	s_cmpk_lt_u32 s78, 0x970
	s_cbranch_scc1 .Lcv_gu_B2
	s_sub_u32 s78, s78, 0x970
	s_lshr_b32 s83, s78, 6
	s_bfe_u32 s93, s78, 0x30003
	s_and_b32 s94, s78, 7
	s_mul_i32 s98, s77, 0x8000000
	s_lshl_b32 s95, s83, 23
	s_add_u32 s98, s98, s95
	s_lshl_b32 s95, s93, 20
	s_add_u32 s98, s98, s95
	s_lshl_b32 s95, s94, 10
	s_add_u32 s98, s98, s95
	s_mul_i32 s99, s77, 0x4000000
	s_add_u32 s99, s99, 0x14400000
	s_lshl_b32 s95, s83, 22
	s_add_u32 s99, s99, s95
	s_lshl_b32 s95, s94, 19
	s_add_u32 s99, s99, s95
	s_lshl_b32 s95, s93, 8
	s_add_u32 s99, s99, s95
	v_readlane_b32 s30, v249, 4
	v_readlane_b32 s31, v249, 5
	s_movk_i32 s56, 0x2000
	s_movk_i32 s57, 0x800
	s_mov_b32 s59, 0x40000
	s_branch .Lcv_fin_B2

; #define PW_SYNC do { asm volatile("s_waitcnt lgkmcnt(0)" ::: "memory"); __builtin_amdgcn_s_barrier(); asm volatile("" ::: "memory"); } while (0)
; __device__ __forceinline__ void ph_weights(const Params& p, LAS unsigned char* lds, const int p0, const int p1, const int wi, const int wn) {
;     ...
;     while (hA) {
;         { PW_TOLDS(dA0, a0, a1); PW_SYNC; const TDesc s0 = dA0, s1 = dA1; PW_LOAD(pi + 2 * wn, dA0, dA1, a0, a1, hA); PW_STORE(s0, s1); PW_SYNC; }
;         if (!hB) break;
;         { PW_TOLDS(dB0, b0, b1); PW_SYNC; const TDesc s0 = dB0, s1 = dB1; PW_LOAD(pi + 3 * wn, dB0, dB1, b0, b1, hB); PW_STORE(s0, s1); PW_SYNC; }
;         pi += 2 * wn;
.Lcv_loop:
	s_and_b32 s8, s9, 1
	s_cmp_eq_u32 s8, 0
	s_cbranch_scc1 .Lcv_done
	s_mov_b64 s[84:85], s[14:15]
	s_mov_b32 s69, s23
	s_mov_b32 s75, s28
	s_mov_b32 s87, s29
	s_mov_b32 s86, s0
	s_add_u32 s0, s0, 1
	s_add_u32 s72, s72, 1
	s_cmp_eq_u32 s72, s73
	s_cselect_b32 s8, s70, 0
	s_cselect_b32 s72, 0, s72
	s_add_u32 s0, s0, s8
	s_cmp_lt_u32 s86, s71
	s_cbranch_scc1 .Lcv_dec_A
	s_andn2_b32 s9, s9, 1
	s_mov_b32 s22, 0
	s_branch .Lcv_ld_A

; #define PW_SYNC do { asm volatile("s_waitcnt lgkmcnt(0)" ::: "memory"); __builtin_amdgcn_s_barrier(); asm volatile("" ::: "memory"); } while (0)
; __device__ __forceinline__ void ph_weights(const Params& p, LAS unsigned char* lds, const int p0, const int p1, const int wi, const int wn) {
;     ...
;     int pi = p0 + wi; bool hA, hB;
;     PW_LOAD(pi, dA0, dA1, a0, a1, hA);
;     PW_LOAD(pi + wn, dB0, dB1, b0, b1, hB);
;     while (hA) {
;         { PW_TOLDS(dA0, a0, a1); PW_SYNC; const TDesc s0 = dA0, s1 = dA1; PW_LOAD(pi + 2 * wn, dA0, dA1, a0, a1, hA); PW_STORE(s0, s1); PW_SYNC; }
;         if (!hB) break;
;         { PW_TOLDS(dB0, b0, b1); PW_SYNC; const TDesc s0 = dB0, s1 = dB1; PW_LOAD(pi + 3 * wn, dB0, dB1, b0, b1, hB); PW_STORE(s0, s1); PW_SYNC; }
.Lcv_nosc1_At:
	v_cvt_pk_bf16_f32 v18, v18, v22
	v_cvt_pk_bf16_f32 v19, v19, v23
	v_cvt_pk_bf16_f32 v20, v20, v24
	v_cvt_pk_bf16_f32 v21, v21, v25
	v_cvt_pk_bf16_f32 v50, v50, v54
	v_cvt_pk_bf16_f32 v51, v51, v55
	v_cvt_pk_bf16_f32 v52, v52, v56
	v_cvt_pk_bf16_f32 v53, v53, v57
	ds_write_b128 v156, v[18:21] offset:16384
	ds_write_b128 v156, v[50:53] offset:49152
	v_cvt_pk_bf16_f32 v26, v26, v30
	v_cvt_pk_bf16_f32 v27, v27, v31
	v_cvt_pk_bf16_f32 v28, v28, v32
	v_cvt_pk_bf16_f32 v29, v29, v33
	v_cvt_pk_bf16_f32 v58, v58, v62
	v_cvt_pk_bf16_f32 v59, v59, v63
	v_cvt_pk_bf16_f32 v60, v60, v64
	v_cvt_pk_bf16_f32 v61, v61, v65
	ds_write_b128 v157, v[26:29] offset:24576
	ds_write_b128 v157, v[58:61] offset:57344
	v_mad_u32_u24 v177, v168, s22, v169
	s_mov_b64 s[88:89], s[12:13]
	s_add_u32 s90, s12, s22
	s_addc_u32 s91, s13, 0
	s_lshl_b32 s92, s22, 5
	global_load_dwordx2 v[138:139], v170, s[20:21]
	global_load_dwordx2 v[140:141], v170, s[20:21] offset:128
	global_load_dwordx2 v[142:143], v170, s[20:21] offset:256
	global_load_dwordx2 v[144:145], v170, s[20:21] offset:384
	global_load_dwordx4 v[2:5], v177, s[88:89] nt
	global_load_dwordx4 v[34:37], v177, s[88:89] offset:512 nt
	global_load_dwordx4 v[6:9], v177, s[90:91] nt
	global_load_dwordx4 v[38:41], v177, s[90:91] offset:512 nt
	s_add_u32 s88, s88, s92
	s_addc_u32 s89, s89, 0
	s_add_u32 s90, s90, s92
	s_addc_u32 s91, s91, 0
	global_load_dwordx4 v[10:13], v177, s[88:89] nt
	global_load_dwordx4 v[42:45], v177, s[88:89] offset:512 nt
	global_load_dwordx4 v[14:17], v177, s[90:91] nt
	global_load_dwordx4 v[46:49], v177, s[90:91] offset:512 nt
	s_add_u32 s88, s88, s92
	s_addc_u32 s89, s89, 0
	s_add_u32 s90, s90, s92
	s_addc_u32 s91, s91, 0
	global_load_dwordx4 v[18:21], v177, s[88:89] nt
	global_load_dwordx4 v[50:53], v177, s[88:89] offset:512 nt
	global_load_dwordx4 v[22:25], v177, s[90:91] nt
	global_load_dwordx4 v[54:57], v177, s[90:91] offset:512 nt
	s_add_u32 s88, s88, s92
	s_addc_u32 s89, s89, 0
	s_add_u32 s90, s90, s92
	s_addc_u32 s91, s91, 0
	global_load_dwordx4 v[26:29], v177, s[88:89] nt
	global_load_dwordx4 v[58:61], v177, s[88:89] offset:512 nt
	global_load_dwordx4 v[30:33], v177, s[90:91] nt
	global_load_dwordx4 v[62:65], v177, s[90:91] offset:512 nt
	s_waitcnt lgkmcnt(0)
	s_barrier
	v_mad_u32_u24 v178, v175, s69, v176
	s_mov_b64 s[88:89], s[84:85]
	s_add_u32 s90, s84, s75
	s_addc_u32 s91, s85, 0
	s_lshl_b32 s92, s69, 5
	ds_read_b32 v228, v162
	ds_read_b32 v229, v162 offset:512
	ds_read_b32 v230, v162 offset:1024
	ds_read_b32 v231, v162 offset:1536
	ds_read_b32 v232, v162 offset:32768
	ds_read_b32 v233, v162 offset:33280
	ds_read_b32 v234, v162 offset:33792
	ds_read_b32 v235, v162 offset:34304
	s_waitcnt lgkmcnt(0)
	ds_read_b32 v204, v163
	ds_read_b32 v205, v163 offset:512
	ds_read_b32 v206, v163 offset:1024
	ds_read_b32 v207, v163 offset:1536
	ds_read_b32 v208, v163 offset:32768
	ds_read_b32 v209, v163 offset:33280
	ds_read_b32 v210, v163 offset:33792
	ds_read_b32 v211, v163 offset:34304
	global_store_dwordx4 v178, v[228:231], s[88:89] nt
	global_store_dwordx4 v178, v[232:235], s[90:91] nt
	s_add_u32 s88, s88, s92
	s_addc_u32 s89, s89, 0
	s_add_u32 s90, s90, s92
	s_addc_u32 s91, s91, 0
	s_waitcnt lgkmcnt(0)
	ds_read_b32 v228, v164
	ds_read_b32 v229, v164 offset:512
	ds_read_b32 v230, v164 offset:1024
	ds_read_b32 v231, v164 offset:1536
	ds_read_b32 v232, v164 offset:32768
	ds_read_b32 v233, v164 offset:33280
	ds_read_b32 v234, v164 offset:33792
	ds_read_b32 v235, v164 offset:34304
	global_store_dwordx4 v178, v[204:207], s[88:89] nt
	global_store_dwordx4 v178, v[208:211], s[90:91] nt
	s_add_u32 s88, s88, s92
	s_addc_u32 s89, s89, 0
	s_add_u32 s90, s90, s92
	s_addc_u32 s91, s91, 0
	s_waitcnt lgkmcnt(0)
	ds_read_b32 v204, v165
	ds_read_b32 v205, v165 offset:512
	ds_read_b32 v206, v165 offset:1024
	ds_read_b32 v207, v165 offset:1536
	ds_read_b32 v208, v165 offset:32768
	ds_read_b32 v209, v165 offset:33280
	ds_read_b32 v210, v165 offset:33792
	ds_read_b32 v211, v165 offset:34304
	global_store_dwordx4 v178, v[228:231], s[88:89] nt
	global_store_dwordx4 v178, v[232:235], s[90:91] nt
	s_add_u32 s88, s88, s92
	s_addc_u32 s89, s89, 0
	s_add_u32 s90, s90, s92
	s_addc_u32 s91, s91, 0
	s_waitcnt lgkmcnt(0)
	global_store_dwordx4 v178, v[204:207], s[88:89] nt
	global_store_dwordx4 v178, v[208:211], s[90:91] nt
	s_and_b32 s8, s9, 2
	s_cmp_eq_u32 s8, 0
	s_cbranch_scc1 .Lcv_done
	s_mov_b64 s[84:85], s[32:33]
	s_mov_b32 s69, s57
	s_mov_b32 s75, s59
	s_mov_b32 s87, s60
	s_mov_b32 s86, s0
	s_add_u32 s0, s0, 1
	s_add_u32 s72, s72, 1
	s_cmp_eq_u32 s72, s73
	s_cselect_b32 s8, s70, 0
	s_cselect_b32 s72, 0, s72
	s_add_u32 s0, s0, s8
	s_cmp_lt_u32 s86, s71
	s_cbranch_scc1 .Lcv_dec_B
	s_andn2_b32 s9, s9, 2
	s_mov_b32 s56, 0
	s_branch .Lcv_ld_B

; #define PW_SYNC do { asm volatile("s_waitcnt lgkmcnt(0)" ::: "memory"); __builtin_amdgcn_s_barrier(); asm volatile("" ::: "memory"); } while (0)
; __device__ __forceinline__ void ph_weights(const Params& p, LAS unsigned char* lds, const int p0, const int p1, const int wi, const int wn) {
;     ...
;     int pi = p0 + wi; bool hA, hB;
;     PW_LOAD(pi, dA0, dA1, a0, a1, hA);
;     PW_LOAD(pi + wn, dB0, dB1, b0, b1, hB);
;     while (hA) {
;         { PW_TOLDS(dA0, a0, a1); PW_SYNC; const TDesc s0 = dA0, s1 = dA1; PW_LOAD(pi + 2 * wn, dA0, dA1, a0, a1, hA); PW_STORE(s0, s1); PW_SYNC; }
;         if (!hB) break;
;         { PW_TOLDS(dB0, b0, b1); PW_SYNC; const TDesc s0 = dB0, s1 = dB1; PW_LOAD(pi + 3 * wn, dB0, dB1, b0, b1, hB); PW_STORE(s0, s1); PW_SYNC; }
;         pi += 2 * wn;
;     }
.Lcv_nosc1_Bt:
	v_cvt_pk_bf16_f32 v82, v82, v86
	v_cvt_pk_bf16_f32 v83, v83, v87
	v_cvt_pk_bf16_f32 v84, v84, v88
	v_cvt_pk_bf16_f32 v85, v85, v89
	v_cvt_pk_bf16_f32 v114, v114, v118
	v_cvt_pk_bf16_f32 v115, v115, v119
	v_cvt_pk_bf16_f32 v116, v116, v120
	v_cvt_pk_bf16_f32 v117, v117, v121
	ds_write_b128 v160, v[82:85] offset:16384
	ds_write_b128 v160, v[114:117] offset:49152
	v_cvt_pk_bf16_f32 v90, v90, v94
	v_cvt_pk_bf16_f32 v91, v91, v95
	v_cvt_pk_bf16_f32 v92, v92, v96
	v_cvt_pk_bf16_f32 v93, v93, v97
	v_cvt_pk_bf16_f32 v122, v122, v126
	v_cvt_pk_bf16_f32 v123, v123, v127
	v_cvt_pk_bf16_f32 v124, v124, v128
	v_cvt_pk_bf16_f32 v125, v125, v129
	ds_write_b128 v161, v[90:93] offset:24576
	ds_write_b128 v161, v[122:125] offset:57344
	v_mad_u32_u24 v177, v168, s56, v169
	s_mov_b64 s[88:89], s[30:31]
	s_add_u32 s90, s30, s56
	s_addc_u32 s91, s31, 0
	s_lshl_b32 s92, s56, 5
	global_load_dwordx2 v[146:147], v170, s[36:37]
	global_load_dwordx2 v[148:149], v170, s[36:37] offset:128
	global_load_dwordx2 v[150:151], v170, s[36:37] offset:256
	global_load_dwordx2 v[152:153], v170, s[36:37] offset:384
	global_load_dwordx4 v[66:69], v177, s[88:89] nt
	global_load_dwordx4 v[98:101], v177, s[88:89] offset:512 nt
	global_load_dwordx4 v[70:73], v177, s[90:91] nt
	global_load_dwordx4 v[102:105], v177, s[90:91] offset:512 nt
	s_add_u32 s88, s88, s92
	s_addc_u32 s89, s89, 0
	s_add_u32 s90, s90, s92
	s_addc_u32 s91, s91, 0
	global_load_dwordx4 v[74:77], v177, s[88:89] nt
	global_load_dwordx4 v[106:109], v177, s[88:89] offset:512 nt
	global_load_dwordx4 v[78:81], v177, s[90:91] nt
	global_load_dwordx4 v[110:113], v177, s[90:91] offset:512 nt
	s_add_u32 s88, s88, s92
	s_addc_u32 s89, s89, 0
	s_add_u32 s90, s90, s92
	s_addc_u32 s91, s91, 0
	global_load_dwordx4 v[82:85], v177, s[88:89] nt
	global_load_dwordx4 v[114:117], v177, s[88:89] offset:512 nt
	global_load_dwordx4 v[86:89], v177, s[90:91] nt
	global_load_dwordx4 v[118:121], v177, s[90:91] offset:512 nt
	s_add_u32 s88, s88, s92
	s_addc_u32 s89, s89, 0
	s_add_u32 s90, s90, s92
	s_addc_u32 s91, s91, 0
	global_load_dwordx4 v[90:93], v177, s[88:89] nt
	global_load_dwordx4 v[122:125], v177, s[88:89] offset:512 nt
	global_load_dwordx4 v[94:97], v177, s[90:91] nt
	global_load_dwordx4 v[126:129], v177, s[90:91] offset:512 nt
	s_waitcnt lgkmcnt(0)
	s_barrier
	v_mad_u32_u24 v178, v175, s69, v176
	s_mov_b64 s[88:89], s[84:85]
	s_add_u32 s90, s84, s75
	s_addc_u32 s91, s85, 0
	s_lshl_b32 s92, s69, 5
	ds_read_b32 v228, v130
	ds_read_b32 v229, v130 offset:512
	ds_read_b32 v230, v130 offset:1024
	ds_read_b32 v231, v130 offset:1536
	ds_read_b32 v232, v130 offset:32768
	ds_read_b32 v233, v130 offset:33280
	ds_read_b32 v234, v130 offset:33792
	ds_read_b32 v235, v130 offset:34304
	s_waitcnt lgkmcnt(0)
	ds_read_b32 v204, v131
	ds_read_b32 v205, v131 offset:512
	ds_read_b32 v206, v131 offset:1024
	ds_read_b32 v207, v131 offset:1536
	ds_read_b32 v208, v131 offset:32768
	ds_read_b32 v209, v131 offset:33280
	ds_read_b32 v210, v131 offset:33792
	ds_read_b32 v211, v131 offset:34304
	global_store_dwordx4 v178, v[228:231], s[88:89] nt
	global_store_dwordx4 v178, v[232:235], s[90:91] nt
	s_add_u32 s88, s88, s92
	s_addc_u32 s89, s89, 0
	s_add_u32 s90, s90, s92
	s_addc_u32 s91, s91, 0
	s_waitcnt lgkmcnt(0)
	ds_read_b32 v228, v132
	ds_read_b32 v229, v132 offset:512
	ds_read_b32 v230, v132 offset:1024
	ds_read_b32 v231, v132 offset:1536
	ds_read_b32 v232, v132 offset:32768
	ds_read_b32 v233, v132 offset:33280
	ds_read_b32 v234, v132 offset:33792
	ds_read_b32 v235, v132 offset:34304
	global_store_dwordx4 v178, v[204:207], s[88:89] nt
	global_store_dwordx4 v178, v[208:211], s[90:91] nt
	s_add_u32 s88, s88, s92
	s_addc_u32 s89, s89, 0
	s_add_u32 s90, s90, s92
	s_addc_u32 s91, s91, 0
	s_waitcnt lgkmcnt(0)
	ds_read_b32 v204, v133
	ds_read_b32 v205, v133 offset:512
	ds_read_b32 v206, v133 offset:1024
	ds_read_b32 v207, v133 offset:1536
	ds_read_b32 v208, v133 offset:32768
	ds_read_b32 v209, v133 offset:33280
	ds_read_b32 v210, v133 offset:33792
	ds_read_b32 v211, v133 offset:34304
	global_store_dwordx4 v178, v[228:231], s[88:89] nt
	global_store_dwordx4 v178, v[232:235], s[90:91] nt
	s_add_u32 s88, s88, s92
	s_addc_u32 s89, s89, 0
	s_add_u32 s90, s90, s92
	s_addc_u32 s91, s91, 0
	s_waitcnt lgkmcnt(0)
	global_store_dwordx4 v178, v[204:207], s[88:89] nt
	global_store_dwordx4 v178, v[208:211], s[90:91] nt
	s_branch .Lcv_loop
